# lru prep gate step: the twelve weight fragments of column tiles 1..3 requested together instead of twelve load-wait-MFMA round trips (on top of v36)
# speedup vs baseline: 1.0035x; 1.0035x over previous
.LBB0_370:
	v_ashrrev_i32_e32 v11, 6, v30
	v_add_u32_e32 v8, v111, v104
	s_waitcnt lgkmcnt(0)
	s_barrier
	v_lshl_add_u32 v22, v11, 8, v8
	ds_read2st64_b32 v[112:113], v22 offset1:1
	ds_read2st64_b32 v[114:115], v22 offset0:2 offset1:3
	ds_read2st64_b32 v[116:117], v22 offset0:8 offset1:9
	ds_read2st64_b32 v[118:119], v22 offset0:10 offset1:11
	ds_read2st64_b32 v[120:121], v22 offset0:16 offset1:17
	ds_read2st64_b32 v[122:123], v22 offset0:18 offset1:19
	ds_read2st64_b32 v[124:125], v22 offset0:24 offset1:25
	ds_read2st64_b32 v[126:127], v22 offset0:26 offset1:27
	ds_read2st64_b32 v[128:129], v22 offset0:32 offset1:33
	ds_read2st64_b32 v[130:131], v22 offset0:34 offset1:35
	ds_read2st64_b32 v[132:133], v22 offset0:40 offset1:41
	ds_read2st64_b32 v[134:135], v22 offset0:42 offset1:43
	ds_read2st64_b32 v[136:137], v22 offset0:48 offset1:49
	ds_read2st64_b32 v[138:139], v22 offset0:50 offset1:51
	ds_read2st64_b32 v[140:141], v22 offset0:56 offset1:57
	ds_read2st64_b32 v[142:143], v22 offset0:58 offset1:59
	v_lshlrev_b32_e32 v9, 1, v31
	s_movk_i32 s0, 0x104
	v_sub_u32_e32 v10, v8, v9
	v_mad_u64_u32 v[8:9], s[0:1], v11, s0, v[8:9]
	s_waitcnt vmcnt(12) lgkmcnt(0)
	v_fma_f32 v23, v15, v112, v14
	v_fmac_f32_e32 v23, v21, v113
	v_mad_u64_u32 v[10:11], s[0:1], v11, s39, v[10:11]
	s_or_b32 s0, s24, s71
	s_ashr_i32 s1, s0, 31
	v_fmac_f32_e32 v23, v12, v114
	v_fmac_f32_e32 v23, v13, v115
	ds_write_b32 v8, v23 offset:17408
	v_bfe_u32 v9, v23, 16, 1
	v_add3_u32 v9, v23, v9, s25
	ds_write_b16_d16_hi v10, v9 offset:34304
	s_lshl_b64 s[0:1], s[0:1], 13
	v_fma_f32 v9, v15, v116, v14
	v_fmac_f32_e32 v9, v21, v117
	s_add_u32 s2, s69, s0
	s_addc_u32 s3, s70, s1
	v_and_b32_e32 v24, 48, v30
	v_mov_b32_e32 v25, v105
	v_fmac_f32_e32 v9, v12, v118
	v_fmac_f32_e32 v9, v13, v119
	ds_write_b32 v8, v9 offset:19488
	v_bfe_u32 v11, v9, 16, 1
	v_add3_u32 v9, v9, v11, s25
	ds_write_b16_d16_hi v10, v9 offset:35456
	s_or_b32 s0, s24, s72
	v_fma_f32 v9, v15, v120, v14
	v_fmac_f32_e32 v9, v21, v121
	s_ashr_i32 s1, s0, 31
	s_lshl_b64 s[0:1], s[0:1], 13
	s_add_u32 s0, s69, s0
	s_addc_u32 s1, s70, s1
	v_fmac_f32_e32 v9, v12, v122
	v_fmac_f32_e32 v9, v13, v123
	ds_write_b32 v8, v9 offset:21568
	v_bfe_u32 v11, v9, 16, 1
	v_add3_u32 v9, v9, v11, s25
	ds_write_b16_d16_hi v10, v9 offset:36608
	s_mov_b32 s14, 0xbfb8aa3b
	v_fma_f32 v9, v15, v124, v14
	v_fmac_f32_e32 v9, v21, v125
	v_or_b32_e32 v47, 16, v35
	v_cmp_gt_u32_e32 vcc, s21, v30
	v_mov_b32_e32 v67, 1.0
	v_mov_b32_e32 v68, 0
	v_fmac_f32_e32 v9, v12, v126
	v_fmac_f32_e32 v9, v13, v127
	ds_write_b32 v8, v9 offset:23648
	v_bfe_u32 v11, v9, 16, 1
	v_add3_u32 v9, v9, v11, s25
	ds_write_b16_d16_hi v10, v9 offset:37760
	v_fma_f32 v9, v15, v128, v14
	v_fmac_f32_e32 v9, v21, v129
	v_fmac_f32_e32 v9, v12, v130
	v_fmac_f32_e32 v9, v13, v131
	ds_write_b32 v8, v9 offset:25728
	v_bfe_u32 v11, v9, 16, 1
	v_add3_u32 v9, v9, v11, s25
	ds_write_b16_d16_hi v10, v9 offset:38912
	v_fma_f32 v9, v15, v132, v14
	v_fmac_f32_e32 v9, v21, v133
	v_fmac_f32_e32 v9, v12, v134
	v_fmac_f32_e32 v9, v13, v135
	ds_write_b32 v8, v9 offset:27808
	v_bfe_u32 v11, v9, 16, 1
	v_add3_u32 v9, v9, v11, s25
	ds_write_b16_d16_hi v10, v9 offset:40064
	v_fma_f32 v9, v15, v136, v14
	v_fmac_f32_e32 v9, v21, v137
	v_fmac_f32_e32 v9, v12, v138
	v_fmac_f32_e32 v9, v13, v139
	ds_write_b32 v8, v9 offset:29888
	v_bfe_u32 v11, v9, 16, 1
	v_add3_u32 v9, v9, v11, s25
	ds_write_b16_d16_hi v10, v9 offset:41216
	v_fmac_f32_e32 v14, v15, v140
	v_fmac_f32_e32 v14, v21, v141
	v_fmac_f32_e32 v14, v12, v142
	v_fmac_f32_e32 v14, v13, v143
	ds_write_b32 v8, v14 offset:31968
	v_bfe_u32 v8, v14, 16, 1
	v_add3_u32 v8, v14, v8, s25
	v_lshrrev_b32_e32 v16, 2, v30
	ds_write_b16_d16_hi v10, v8 offset:42368
	v_or_b32_e32 v8, s34, v35
	v_and_or_b32 v21, v16, 12, s34
	v_lshlrev_b32_e32 v16, 7, v35
	v_mov_b32_e32 v17, v105
	v_mul_u32_u24_e32 v8, 0x90, v8
	v_lshl_add_u64 v[22:23], s[2:3], 0, v[16:17]
	s_waitcnt lgkmcnt(0)
	s_barrier
	v_add3_u32 v8, v111, v8, v24
	v_lshl_add_u64 v[22:23], v[22:23], 0, v[24:25]
	ds_read_b128 v[12:15], v8 offset:34304
	ds_read_b128 v[8:11], v8 offset:34368
	global_load_dwordx4 v[36:39], v[22:23], off
	global_load_dwordx4 v[48:51], v[22:23], off offset:64
	v_lshl_add_u64 v[16:17], s[0:1], 0, v[16:17]
	v_lshl_add_u64 v[16:17], v[16:17], 0, v[24:25]
	v_lshlrev_b32_e32 v42, 6, v21
	s_waitcnt vmcnt(1) lgkmcnt(1)
	v_mfma_f32_16x16x32_bf16 v[36:39], v[12:15], v[36:39], 0
	global_load_dwordx4 v[52:55], v[16:17], off offset:64
	s_waitcnt vmcnt(1) lgkmcnt(0)
	v_mfma_f32_16x16x32_bf16 v[48:51], v[8:11], v[48:51], v[36:39]
	s_nop 4
	global_load_dwordx4 v[36:39], v[16:17], off
	s_mov_b64 s[100:101], 0x1000
	v_lshl_add_u64 v[180:181], v[22:23], 0, s[100:101]
	v_lshl_add_u64 v[72:73], v[16:17], 0, s[100:101]
	global_load_dwordx4 v[216:219], v[22:23], off offset:2048
	global_load_dwordx4 v[220:223], v[22:23], off offset:2112
	global_load_dwordx4 v[224:227], v[16:17], off offset:2048
	global_load_dwordx4 v[228:231], v[16:17], off offset:2112
	global_load_dwordx4 v[232:235], v[180:181], off
	global_load_dwordx4 v[236:239], v[180:181], off offset:64
	global_load_dwordx4 v[240:243], v[72:73], off
	global_load_dwordx4 v[244:247], v[72:73], off offset:64
	global_load_dwordx4 v[248:251], v[180:181], off offset:2048
	global_load_dwordx4 v[200:203], v[180:181], off offset:2112
	global_load_dwordx4 v[204:207], v[72:73], off offset:2048
	global_load_dwordx4 v[208:211], v[72:73], off offset:2112
	v_mul_f32_e64 v17, |v20|, s14
	s_nop 0
	v_add_f32_e32 v22, v18, v48
	v_mul_f32_e32 v22, 0xbfb8aa3b, v22
	v_exp_f32_e32 v17, v17
	v_exp_f32_e32 v22, v22
	v_max_f32_e64 v16, -v20, -v20
	v_max_f32_e32 v16, 0, v16
	v_add_f32_e32 v17, 1.0, v17
	v_add_f32_e32 v22, 1.0, v22
	v_log_f32_e32 v17, v17
	v_rcp_f32_e32 v22, v22
	v_or_b32_e32 v20, s73, v35
	v_lshlrev_b32_e32 v48, 7, v47
	v_fmac_f32_e32 v16, 0x3f317218, v17
	v_mul_f32_e32 v22, 0xc1000000, v22
	v_mul_f32_e32 v22, v16, v22
	v_mul_f32_e32 v22, 0x3fb8aa3b, v22
	v_exp_f32_e32 v22, v22
	v_lshlrev_b32_e32 v17, 2, v35
	s_waitcnt vmcnt(12)
	v_mfma_f32_16x16x32_bf16 v[36:39], v[12:15], v[36:39], 0
	v_mfma_f32_16x16x32_bf16 v[52:55], v[8:11], v[52:55], v[36:39]
	s_nop 6
	v_fma_f32 v36, -v22, v22, 1.0
	v_max_f32_e32 v36, 0, v36
	v_add_f32_e32 v23, v19, v52
	v_mul_f32_e32 v23, 0xbfb8aa3b, v23
	v_exp_f32_e32 v23, v23
	v_sqrt_f32_e32 v36, v36
	v_or_b32_e32 v39, 64, v42
	v_or_b32_e32 v38, 0x80, v42
	v_add_f32_e32 v23, 1.0, v23
	v_rcp_f32_e32 v23, v23
	v_or_b32_e32 v37, 0xc0, v42
	v_mul_f32_e32 v23, v23, v36
	v_mul_u32_u24_e32 v36, 0x104, v21
	v_add3_u32 v36, v111, v17, v36
	ds_read_b32 v144, v36 offset:17408
	ds_read_b32 v145, v36 offset:17668
	ds_read_b32 v146, v36 offset:17928
	ds_read_b32 v147, v36 offset:18188
	ds_read_b32 v148, v36 offset:17472
	ds_read_b32 v149, v36 offset:17732
	ds_read_b32 v150, v36 offset:17992
	ds_read_b32 v151, v36 offset:18252
	ds_read_b32 v152, v36 offset:17536
	ds_read_b32 v153, v36 offset:17796
	ds_read_b32 v154, v36 offset:18056
	ds_read_b32 v155, v36 offset:18316
	ds_read_b32 v156, v36 offset:17600
	ds_read_b32 v157, v36 offset:17860
	ds_read_b32 v158, v36 offset:18120
	ds_read_b32 v159, v36 offset:18380
	v_or_b32_e32 v21, v42, v20
	v_lshlrev_b32_e32 v21, 2, v21
	s_waitcnt lgkmcnt(0)
	v_mul_f32_e32 v17, v144, v23
	v_add_u32_e32 v23, v111, v21
	v_add_u32_e32 v21, v28, v21
	ds_write_b32 v23, v22 offset:43520
	ds_write_b32 v21, v17
	v_add_f32_e32 v17, v18, v49
	v_mul_f32_e32 v17, 0xbfb8aa3b, v17
	v_exp_f32_e32 v17, v17
	v_add_f32_e32 v21, v19, v53
	v_mul_f32_e32 v21, 0xbfb8aa3b, v21
	v_exp_f32_e32 v21, v21
	v_add_f32_e32 v17, 1.0, v17
	v_rcp_f32_e32 v17, v17
	v_mov_b32_e32 v49, v105
	v_add_f32_e32 v21, 1.0, v21
	v_rcp_f32_e32 v21, v21
	v_mul_f32_e32 v17, 0xc1000000, v17
	v_mul_f32_e32 v17, v16, v17
	v_mul_f32_e32 v17, 0x3fb8aa3b, v17
	v_exp_f32_e32 v17, v17
	s_nop 0
	v_fma_f32 v22, -v17, v17, 1.0
	v_max_f32_e32 v22, 0, v22
	v_sqrt_f32_e32 v22, v22
	s_nop 0
	v_mul_f32_e32 v21, v21, v22
	v_mul_f32_e32 v21, v145, v21
	v_or_b32_e32 v22, v39, v20
	v_lshlrev_b32_e32 v22, 2, v22
	v_add_u32_e32 v23, v111, v22
	ds_write_b32 v23, v17 offset:43520
	v_add_u32_e32 v17, v28, v22
	ds_write_b32 v17, v21
	v_add_f32_e32 v17, v18, v50
	v_mul_f32_e32 v17, 0xbfb8aa3b, v17
	v_exp_f32_e32 v17, v17
	v_add_f32_e32 v21, v19, v54
	v_mul_f32_e32 v21, 0xbfb8aa3b, v21
	v_exp_f32_e32 v21, v21
	v_add_f32_e32 v17, 1.0, v17
	v_rcp_f32_e32 v17, v17
	v_add_f32_e32 v21, 1.0, v21
	v_rcp_f32_e32 v21, v21
	v_mul_f32_e32 v17, 0xc1000000, v17
	v_mul_f32_e32 v17, v16, v17
	v_mul_f32_e32 v17, 0x3fb8aa3b, v17
	v_exp_f32_e32 v17, v17
	s_nop 0
	v_fma_f32 v22, -v17, v17, 1.0
	v_max_f32_e32 v22, 0, v22
	v_sqrt_f32_e32 v22, v22
	s_nop 0
	v_mul_f32_e32 v21, v21, v22
	v_mul_f32_e32 v21, v146, v21
	v_or_b32_e32 v22, v38, v20
	v_lshlrev_b32_e32 v22, 2, v22
	v_add_u32_e32 v23, v111, v22
	ds_write_b32 v23, v17 offset:43520
	v_add_u32_e32 v17, v28, v22
	ds_write_b32 v17, v21
	v_add_f32_e32 v17, v18, v51
	v_mul_f32_e32 v17, 0xbfb8aa3b, v17
	v_exp_f32_e32 v17, v17
	v_add_f32_e32 v18, v19, v55
	v_mul_f32_e32 v18, 0xbfb8aa3b, v18
	v_exp_f32_e32 v18, v18
	v_add_f32_e32 v17, 1.0, v17
	v_rcp_f32_e32 v17, v17
	v_add_f32_e32 v18, 1.0, v18
	v_rcp_f32_e32 v18, v18
	v_mul_f32_e32 v17, 0xc1000000, v17
	v_mul_f32_e32 v16, v16, v17
	v_mul_f32_e32 v16, 0x3fb8aa3b, v16
	v_exp_f32_e32 v16, v16
	s_nop 0
	v_fma_f32 v17, -v16, v16, 1.0
	v_max_f32_e32 v17, 0, v17
	v_sqrt_f32_e32 v17, v17
	s_nop 0
	v_mul_f32_e32 v17, v18, v17
	v_mul_f32_e32 v17, v147, v17
	v_or_b32_e32 v18, v37, v20
	v_lshlrev_b32_e32 v18, 2, v18
	v_add_u32_e32 v19, v111, v18
	ds_write_b32 v19, v16 offset:43520
	v_add_u32_e32 v16, v28, v18
	ds_write_b32 v16, v17
	v_lshl_add_u64 v[16:17], s[2:3], 0, v[48:49]
	v_lshl_add_u64 v[20:21], v[16:17], 0, v[24:25]
	s_waitcnt vmcnt(0)
	v_mfma_f32_16x16x32_bf16 v[16:19], v[12:15], v[216:219], 0
	s_waitcnt vmcnt(0)
	v_mfma_f32_16x16x32_bf16 v[16:19], v[8:11], v[220:223], v[16:19]
	v_lshl_add_u64 v[20:21], s[0:1], 0, v[48:49]
	v_lshl_add_u64 v[48:49], v[20:21], 0, v[24:25]
	s_waitcnt vmcnt(0)
	v_mfma_f32_16x16x32_bf16 v[20:23], v[12:15], v[224:227], 0
	s_nop 1
	v_add_f32_e32 v16, v45, v16
	v_mul_f32_e32 v16, 0xbfb8aa3b, v16
	s_waitcnt vmcnt(0)
	v_mfma_f32_16x16x32_bf16 v[20:23], v[8:11], v[228:231], v[20:23]
	v_max_f32_e64 v48, -v46, -v46
	v_mul_f32_e64 v46, |v46|, s14
	v_exp_f32_e32 v46, v46
	v_exp_f32_e32 v16, v16
	v_max_f32_e32 v49, 0, v48
	s_nop 2
	v_add_f32_e32 v20, v44, v20
	v_add_f32_e32 v46, 1.0, v46
	v_add_f32_e32 v16, 1.0, v16
	v_log_f32_e32 v46, v46
	v_rcp_f32_e32 v16, v16
	v_mul_f32_e32 v20, 0xbfb8aa3b, v20
	v_exp_f32_e32 v20, v20
	v_fmac_f32_e32 v49, 0x3f317218, v46
	v_mul_f32_e32 v16, 0xc1000000, v16
	v_mul_f32_e32 v16, v49, v16
	v_mul_f32_e32 v16, 0x3fb8aa3b, v16
	v_exp_f32_e32 v16, v16
	v_add_f32_e32 v20, 1.0, v20
	v_rcp_f32_e32 v20, v20
	v_add_u32_e32 v51, s73, v35
	v_fma_f32 v46, -v16, v16, 1.0
	v_max_f32_e32 v46, 0, v46
	v_sqrt_f32_e32 v46, v46
	v_or_b32_e32 v50, s73, v47
	v_add_u32_e32 v47, v42, v51
	v_lshl_add_u32 v48, v47, 2, v111
	v_mul_f32_e32 v20, v20, v46
	ds_write_b32 v48, v16 offset:43584
	v_mul_f32_e32 v20, v148, v20
	v_or_b32_e32 v46, v42, v50
	v_lshl_add_u32 v16, v46, 2, v28
	ds_write_b32 v16, v20
	v_add_f32_e32 v16, v45, v17
	v_mul_f32_e32 v16, 0xbfb8aa3b, v16
	v_exp_f32_e32 v16, v16
	v_add_f32_e32 v17, v44, v21
	v_mul_f32_e32 v17, 0xbfb8aa3b, v17
	v_exp_f32_e32 v17, v17
	v_add_f32_e32 v16, 1.0, v16
	v_rcp_f32_e32 v16, v16
	v_add_u32_e32 v21, v39, v51
	v_add_f32_e32 v17, 1.0, v17
	v_rcp_f32_e32 v17, v17
	v_mul_f32_e32 v16, 0xc1000000, v16
	v_mul_f32_e32 v16, v49, v16
	v_mul_f32_e32 v16, 0x3fb8aa3b, v16
	v_exp_f32_e32 v16, v16
	v_lshl_add_u32 v47, v21, 2, v111
	v_fma_f32 v20, -v16, v16, 1.0
	v_max_f32_e32 v20, 0, v20
	v_sqrt_f32_e32 v20, v20
	s_nop 0
	v_mul_f32_e32 v17, v17, v20
	ds_write_b32 v47, v16 offset:43584
	v_mul_f32_e32 v17, v149, v17
	v_or_b32_e32 v20, v39, v50
	v_lshl_add_u32 v16, v20, 2, v28
	ds_write_b32 v16, v17
	v_add_f32_e32 v16, v45, v18
	v_mul_f32_e32 v16, 0xbfb8aa3b, v16
	v_exp_f32_e32 v16, v16
	v_add_f32_e32 v17, v44, v22
	v_mul_f32_e32 v17, 0xbfb8aa3b, v17
	v_exp_f32_e32 v17, v17
	v_add_f32_e32 v16, 1.0, v16
	v_rcp_f32_e32 v16, v16
	v_add_u32_e32 v20, v38, v51
	v_add_f32_e32 v17, 1.0, v17
	v_rcp_f32_e32 v17, v17
	v_mul_f32_e32 v16, 0xc1000000, v16
	v_mul_f32_e32 v16, v49, v16
	v_mul_f32_e32 v16, 0x3fb8aa3b, v16
	v_exp_f32_e32 v16, v16
	v_lshl_add_u32 v46, v20, 2, v111
	v_fma_f32 v18, -v16, v16, 1.0
	v_max_f32_e32 v18, 0, v18
	v_sqrt_f32_e32 v18, v18
	s_nop 0
	v_mul_f32_e32 v17, v17, v18
	ds_write_b32 v46, v16 offset:43584
	v_mul_f32_e32 v17, v150, v17
	v_or_b32_e32 v18, v38, v50
	v_lshl_add_u32 v16, v18, 2, v28
	ds_write_b32 v16, v17
	v_add_f32_e32 v16, v45, v19
	v_mul_f32_e32 v16, 0xbfb8aa3b, v16
	v_exp_f32_e32 v16, v16
	v_add_f32_e32 v17, v44, v23
	v_mul_f32_e32 v17, 0xbfb8aa3b, v17
	v_exp_f32_e32 v17, v17
	v_add_f32_e32 v16, 1.0, v16
	v_rcp_f32_e32 v16, v16
	v_add_u32_e32 v19, v37, v51
	v_add_f32_e32 v17, 1.0, v17
	v_rcp_f32_e32 v17, v17
	v_mul_f32_e32 v16, 0xc1000000, v16
	v_mul_f32_e32 v16, v49, v16
	v_mul_f32_e32 v16, 0x3fb8aa3b, v16
	v_exp_f32_e32 v16, v16
	v_lshl_add_u32 v44, v19, 2, v111
	v_or_b32_e32 v45, 32, v35
	v_mov_b32_e32 v51, v105
	v_fma_f32 v18, -v16, v16, 1.0
	v_max_f32_e32 v18, 0, v18
	v_sqrt_f32_e32 v18, v18
	v_max_f32_e64 v49, -v43, -v43
	v_mul_f32_e64 v43, |v43|, s14
	v_exp_f32_e32 v43, v43
	v_mul_f32_e32 v17, v17, v18
	ds_write_b32 v44, v16 offset:43584
	v_add_f32_e32 v43, 1.0, v43
	v_log_f32_e32 v43, v43
	v_max_f32_e32 v49, 0, v49
	v_mul_f32_e32 v17, v151, v17
	v_or_b32_e32 v18, v37, v50
	v_lshl_add_u32 v16, v18, 2, v28
	v_lshlrev_b32_e32 v50, 7, v45
	ds_write_b32 v16, v17
	v_lshl_add_u64 v[16:17], s[2:3], 0, v[50:51]
	v_lshl_add_u64 v[20:21], v[16:17], 0, v[24:25]
	s_waitcnt vmcnt(0)
	v_mfma_f32_16x16x32_bf16 v[16:19], v[12:15], v[232:235], 0
	v_fmac_f32_e32 v49, 0x3f317218, v43
	v_or_b32_e32 v43, s73, v45
	s_waitcnt vmcnt(0)
	v_mfma_f32_16x16x32_bf16 v[16:19], v[8:11], v[236:239], v[16:19]
	v_lshl_add_u64 v[20:21], s[0:1], 0, v[50:51]
	v_lshl_add_u64 v[50:51], v[20:21], 0, v[24:25]
	s_nop 4
	v_add_f32_e32 v16, v41, v16
	v_mul_f32_e32 v16, 0xbfb8aa3b, v16
	v_exp_f32_e32 v16, v16
	s_waitcnt vmcnt(1)
	v_mfma_f32_16x16x32_bf16 v[20:23], v[12:15], v[240:243], 0
	v_add_f32_e32 v16, 1.0, v16
	v_rcp_f32_e32 v16, v16
	v_or_b32_e32 v35, 48, v35
	s_waitcnt vmcnt(0)
	v_mfma_f32_16x16x32_bf16 v[20:23], v[8:11], v[244:247], v[20:23]
	v_mul_f32_e32 v16, 0xc1000000, v16
	v_mul_f32_e32 v16, v49, v16
	v_mul_f32_e32 v16, 0x3fb8aa3b, v16
	v_exp_f32_e32 v16, v16
	s_nop 3
	v_add_f32_e32 v20, v40, v20
	v_mul_f32_e32 v20, 0xbfb8aa3b, v20
	v_exp_f32_e32 v20, v20
	v_fma_f32 v45, -v16, v16, 1.0
	v_max_f32_e32 v45, 0, v45
	v_sqrt_f32_e32 v45, v45
	v_add_f32_e32 v20, 1.0, v20
	v_rcp_f32_e32 v20, v20
	s_nop 0
	v_mul_f32_e32 v20, v20, v45
	ds_write_b32 v48, v16 offset:43648
	v_mul_f32_e32 v20, v152, v20
	v_or_b32_e32 v45, v42, v43
	v_lshl_add_u32 v16, v45, 2, v28
	ds_write_b32 v16, v20
	v_add_f32_e32 v16, v41, v17
	v_mul_f32_e32 v16, 0xbfb8aa3b, v16
	v_exp_f32_e32 v16, v16
	v_add_f32_e32 v17, v40, v21
	v_mul_f32_e32 v17, 0xbfb8aa3b, v17
	v_exp_f32_e32 v17, v17
	v_add_f32_e32 v16, 1.0, v16
	v_rcp_f32_e32 v16, v16
	v_add_f32_e32 v17, 1.0, v17
	v_rcp_f32_e32 v17, v17
	v_mul_f32_e32 v16, 0xc1000000, v16
	v_mul_f32_e32 v16, v49, v16
	v_mul_f32_e32 v16, 0x3fb8aa3b, v16
	v_exp_f32_e32 v16, v16
	s_nop 0
	v_fma_f32 v20, -v16, v16, 1.0
	v_max_f32_e32 v20, 0, v20
	v_sqrt_f32_e32 v20, v20
	s_nop 0
	v_mul_f32_e32 v17, v17, v20
	ds_write_b32 v47, v16 offset:43648
	v_mul_f32_e32 v17, v153, v17
	v_or_b32_e32 v20, v39, v43
	v_lshl_add_u32 v16, v20, 2, v28
	ds_write_b32 v16, v17
	v_add_f32_e32 v16, v41, v18
	v_mul_f32_e32 v16, 0xbfb8aa3b, v16
	v_exp_f32_e32 v16, v16
	v_add_f32_e32 v17, v40, v22
	v_mul_f32_e32 v17, 0xbfb8aa3b, v17
	v_exp_f32_e32 v17, v17
	v_add_f32_e32 v16, 1.0, v16
	v_rcp_f32_e32 v16, v16
	v_add_f32_e32 v17, 1.0, v17
	v_rcp_f32_e32 v17, v17
	v_mul_f32_e32 v16, 0xc1000000, v16
	v_mul_f32_e32 v16, v49, v16
	v_mul_f32_e32 v16, 0x3fb8aa3b, v16
	v_exp_f32_e32 v16, v16
	s_nop 0
	v_fma_f32 v18, -v16, v16, 1.0
	v_max_f32_e32 v18, 0, v18
	v_sqrt_f32_e32 v18, v18
	s_nop 0
	v_mul_f32_e32 v17, v17, v18
	ds_write_b32 v46, v16 offset:43648
	v_mul_f32_e32 v17, v154, v17
	v_or_b32_e32 v18, v38, v43
	v_lshl_add_u32 v16, v18, 2, v28
	ds_write_b32 v16, v17
	v_add_f32_e32 v16, v41, v19
	v_mul_f32_e32 v16, 0xbfb8aa3b, v16
	v_exp_f32_e32 v16, v16
	v_add_f32_e32 v17, v40, v23
	v_mul_f32_e32 v17, 0xbfb8aa3b, v17
	v_exp_f32_e32 v17, v17
	v_add_f32_e32 v16, 1.0, v16
	v_rcp_f32_e32 v16, v16
	v_lshlrev_b32_e32 v40, 7, v35
	v_add_f32_e32 v17, 1.0, v17
	v_rcp_f32_e32 v17, v17
	v_mul_f32_e32 v16, 0xc1000000, v16
	v_mul_f32_e32 v16, v49, v16
	v_mul_f32_e32 v16, 0x3fb8aa3b, v16
	v_exp_f32_e32 v16, v16
	v_mov_b32_e32 v41, v105
	v_fma_f32 v18, -v16, v16, 1.0
	v_max_f32_e32 v18, 0, v18
	v_sqrt_f32_e32 v18, v18
	s_nop 0
	v_mul_f32_e32 v17, v17, v18
	ds_write_b32 v44, v16 offset:43648
	v_mul_f32_e32 v17, v155, v17
	v_or_b32_e32 v18, v37, v43
	v_lshl_add_u32 v16, v18, 2, v28
	ds_write_b32 v16, v17
	v_lshl_add_u64 v[16:17], s[2:3], 0, v[40:41]
	v_lshl_add_u64 v[20:21], v[16:17], 0, v[24:25]
	s_waitcnt vmcnt(0)
	v_mfma_f32_16x16x32_bf16 v[16:19], v[12:15], v[248:251], 0
	s_waitcnt vmcnt(0)
	v_mfma_f32_16x16x32_bf16 v[16:19], v[8:11], v[200:203], v[16:19]
	v_lshl_add_u64 v[20:21], s[0:1], 0, v[40:41]
	v_lshl_add_u64 v[24:25], v[20:21], 0, v[24:25]
	s_waitcnt vmcnt(0)
	v_mfma_f32_16x16x32_bf16 v[12:15], v[12:15], v[204:207], 0
	s_waitcnt vmcnt(0)
	v_mfma_f32_16x16x32_bf16 v[8:11], v[8:11], v[208:211], v[12:15]
	s_nop 4
	v_add_f32_e32 v14, v33, v16
	v_mul_f32_e64 v13, |v34|, s14
	v_mul_f32_e32 v14, 0xbfb8aa3b, v14
	v_exp_f32_e32 v13, v13
	v_exp_f32_e32 v14, v14
	v_max_f32_e64 v12, -v34, -v34
	v_max_f32_e32 v12, 0, v12
	v_add_f32_e32 v13, 1.0, v13
	v_add_f32_e32 v14, 1.0, v14
	v_log_f32_e32 v13, v13
	v_rcp_f32_e32 v14, v14
	v_add_f32_e32 v8, v32, v8
	v_mul_f32_e32 v8, 0xbfb8aa3b, v8
	v_fmac_f32_e32 v12, 0x3f317218, v13
	v_mul_f32_e32 v14, 0xc1000000, v14
	v_mul_f32_e32 v14, v12, v14
	v_mul_f32_e32 v14, 0x3fb8aa3b, v14
	v_exp_f32_e32 v14, v14
	v_exp_f32_e32 v8, v8
	v_or_b32_e32 v13, s73, v35
	v_add_f32_e32 v9, v32, v9
	v_fma_f32 v15, -v14, v14, 1.0
	v_add_f32_e32 v8, 1.0, v8
	v_max_f32_e32 v15, 0, v15
	v_rcp_f32_e32 v8, v8
	v_sqrt_f32_e32 v15, v15
	v_mul_f32_e32 v9, 0xbfb8aa3b, v9
	v_exp_f32_e32 v9, v9
	v_mul_f32_e32 v8, v8, v15
	ds_write_b32 v48, v14 offset:43712
	v_add_f32_e32 v9, 1.0, v9
	v_rcp_f32_e32 v9, v9
	v_mul_f32_e32 v8, v156, v8
	v_or_b32_e32 v15, v42, v13
	v_lshl_add_u32 v14, v15, 2, v28
	ds_write_b32 v14, v8
	v_add_f32_e32 v8, v33, v17
	v_mul_f32_e32 v8, 0xbfb8aa3b, v8
	v_exp_f32_e32 v8, v8
	s_nop 0
	v_add_f32_e32 v8, 1.0, v8
	v_rcp_f32_e32 v8, v8
	s_nop 0
	v_mul_f32_e32 v8, 0xc1000000, v8
	v_mul_f32_e32 v8, v12, v8
	v_mul_f32_e32 v8, 0x3fb8aa3b, v8
	v_exp_f32_e32 v8, v8
	s_nop 0
	v_fma_f32 v14, -v8, v8, 1.0
	v_max_f32_e32 v14, 0, v14
	v_sqrt_f32_e32 v14, v14
	s_nop 0
	v_mul_f32_e32 v9, v9, v14
	ds_write_b32 v47, v8 offset:43712
	v_mul_f32_e32 v9, v157, v9
	v_or_b32_e32 v14, v39, v13
	v_lshl_add_u32 v8, v14, 2, v28
	ds_write_b32 v8, v9
	v_add_f32_e32 v8, v33, v18
	v_mul_f32_e32 v8, 0xbfb8aa3b, v8
	v_exp_f32_e32 v8, v8
	v_add_f32_e32 v9, v32, v10
	v_mul_f32_e32 v9, 0xbfb8aa3b, v9
	v_exp_f32_e32 v9, v9
	v_add_f32_e32 v8, 1.0, v8
	v_rcp_f32_e32 v8, v8
	v_add_f32_e32 v9, 1.0, v9
	v_rcp_f32_e32 v9, v9
	v_mul_f32_e32 v8, 0xc1000000, v8
	v_mul_f32_e32 v8, v12, v8
	v_mul_f32_e32 v8, 0x3fb8aa3b, v8
	v_exp_f32_e32 v8, v8
	s_nop 0
	v_fma_f32 v10, -v8, v8, 1.0
	v_max_f32_e32 v10, 0, v10
	v_sqrt_f32_e32 v10, v10
	s_nop 0
	v_mul_f32_e32 v9, v9, v10
	ds_write_b32 v46, v8 offset:43712
	v_mul_f32_e32 v9, v158, v9
	v_or_b32_e32 v10, v38, v13
	v_lshl_add_u32 v8, v10, 2, v28
	ds_write_b32 v8, v9
	v_add_f32_e32 v8, v33, v19
	v_mul_f32_e32 v8, 0xbfb8aa3b, v8
	v_exp_f32_e32 v8, v8
	v_add_f32_e32 v9, v32, v11
	v_mul_f32_e32 v9, 0xbfb8aa3b, v9
	v_exp_f32_e32 v9, v9
	v_add_f32_e32 v8, 1.0, v8
	v_rcp_f32_e32 v8, v8
	v_add_f32_e32 v9, 1.0, v9
	v_rcp_f32_e32 v9, v9
	v_mul_f32_e32 v8, 0xc1000000, v8
	v_mul_f32_e32 v8, v12, v8
	v_mul_f32_e32 v8, 0x3fb8aa3b, v8
	v_exp_f32_e32 v8, v8
	v_ashrrev_i32_e32 v12, 8, v30
	v_fma_f32 v10, -v8, v8, 1.0
	v_max_f32_e32 v10, 0, v10
	v_sqrt_f32_e32 v10, v10
	s_nop 0
	v_mul_f32_e32 v9, v9, v10
	ds_write_b32 v44, v8 offset:43712
	v_mul_f32_e32 v9, v159, v9
	v_or_b32_e32 v10, v37, v13
	v_lshl_add_u32 v8, v10, 2, v28
	ds_write_b32 v8, v9
	v_bfe_u32 v8, v30, 6, 2
	v_lshlrev_b32_e32 v9, 4, v8
	v_xor_b32_e32 v10, 63, v9
	v_cndmask_b32_e32 v25, v10, v9, vcc
	v_lshl_or_b32 v10, v12, 14, v104
	v_lshl_or_b32 v11, v25, 8, v10
	s_waitcnt lgkmcnt(0)
	s_barrier
	v_add_u32_e32 v13, v111, v11
	v_add_u32_e32 v11, v28, v11
	ds_read_b32 v17, v13 offset:43520
	ds_read_b32 v22, v11
	v_or_b32_e32 v11, 1, v9
	v_xor_b32_e32 v177, 62, v9
	v_cndmask_b32_e32 v19, v177, v11, vcc
	v_lshl_or_b32 v11, v19, 8, v10
	v_add_u32_e32 v179, v111, v11
	v_add_u32_e32 v11, v28, v11
	ds_read_b32 v15, v11
	ds_read_b32 v161, v179 offset:43520
	v_or_b32_e32 v11, 2, v9
	v_xor_b32_e32 v176, 61, v9
	v_cndmask_b32_e32 v20, v176, v11, vcc
	v_lshl_or_b32 v11, v20, 8, v10
	v_add_u32_e32 v178, v111, v11
	v_add_u32_e32 v11, v28, v11
	ds_read_b32 v16, v11
	ds_read_b32 v162, v178 offset:43520
	v_or_b32_e32 v11, 3, v9
	v_xor_b32_e32 v177, 60, v9
	v_cndmask_b32_e32 v21, v177, v11, vcc
	v_lshl_or_b32 v11, v21, 8, v10
	v_add_u32_e32 v179, v111, v11
	v_add_u32_e32 v11, v28, v11
	ds_read_b32 v18, v11
	ds_read_b32 v163, v179 offset:43520
	v_or_b32_e32 v11, 4, v9
	v_xor_b32_e32 v176, 59, v9
	v_cndmask_b32_e32 v36, v176, v11, vcc
	v_lshl_or_b32 v11, v36, 8, v10
	v_add_u32_e32 v178, v111, v11
	v_add_u32_e32 v11, v28, v11
	ds_read_b32 v33, v11
	ds_read_b32 v164, v178 offset:43520
	v_or_b32_e32 v11, 5, v9
	v_xor_b32_e32 v177, 58, v9
	v_cndmask_b32_e32 v37, v177, v11, vcc
	v_lshl_or_b32 v11, v37, 8, v10
	v_add_u32_e32 v179, v111, v11
	v_add_u32_e32 v11, v28, v11
	ds_read_b32 v34, v11
	ds_read_b32 v165, v179 offset:43520
	v_or_b32_e32 v11, 6, v9
	v_xor_b32_e32 v176, 57, v9
	v_cndmask_b32_e32 v39, v176, v11, vcc
	v_lshl_or_b32 v11, v39, 8, v10
	v_add_u32_e32 v178, v111, v11
	v_add_u32_e32 v11, v28, v11
	ds_read_b32 v35, v11
	ds_read_b32 v166, v178 offset:43520
	v_or_b32_e32 v11, 7, v9
	v_xor_b32_e32 v177, 56, v9
	v_cndmask_b32_e32 v45, v177, v11, vcc
	v_lshl_or_b32 v11, v45, 8, v10
	v_add_u32_e32 v179, v111, v11
	v_add_u32_e32 v11, v28, v11
	ds_read_b32 v42, v11
	ds_read_b32 v167, v179 offset:43520
	v_or_b32_e32 v11, 8, v9
	v_xor_b32_e32 v176, 55, v9
	v_cndmask_b32_e32 v46, v176, v11, vcc
	v_lshl_or_b32 v11, v46, 8, v10
	v_add_u32_e32 v178, v111, v11
	v_add_u32_e32 v11, v28, v11
	ds_read_b32 v43, v11
	ds_read_b32 v168, v178 offset:43520
	v_or_b32_e32 v11, 9, v9
	v_xor_b32_e32 v177, 54, v9
	v_cndmask_b32_e32 v48, v177, v11, vcc
	v_lshl_or_b32 v11, v48, 8, v10
	v_add_u32_e32 v179, v111, v11
	v_add_u32_e32 v11, v28, v11
	ds_read_b32 v44, v11
	ds_read_b32 v169, v179 offset:43520
	v_or_b32_e32 v11, 10, v9
	v_xor_b32_e32 v176, 53, v9
	v_cndmask_b32_e32 v54, v176, v11, vcc
	v_lshl_or_b32 v11, v54, 8, v10
	v_add_u32_e32 v178, v111, v11
	v_add_u32_e32 v11, v28, v11
	ds_read_b32 v51, v11
	ds_read_b32 v170, v178 offset:43520
	v_or_b32_e32 v11, 11, v9
	v_xor_b32_e32 v177, 52, v9
	v_cndmask_b32_e32 v55, v177, v11, vcc
	v_lshl_or_b32 v11, v55, 8, v10
	v_add_u32_e32 v179, v111, v11
	v_add_u32_e32 v11, v28, v11
	ds_read_b32 v52, v11
	ds_read_b32 v171, v179 offset:43520
	v_or_b32_e32 v11, 12, v9
	v_xor_b32_e32 v176, 51, v9
	v_cndmask_b32_e32 v57, v176, v11, vcc
	v_lshl_or_b32 v11, v57, 8, v10
	v_add_u32_e32 v178, v111, v11
	v_add_u32_e32 v11, v28, v11
	ds_read_b32 v53, v11
	ds_read_b32 v172, v178 offset:43520
	v_or_b32_e32 v11, 13, v9
	v_xor_b32_e32 v177, 50, v9
	v_cndmask_b32_e32 v62, v177, v11, vcc
	v_lshl_or_b32 v11, v62, 8, v10
	v_add_u32_e32 v179, v111, v11
	v_add_u32_e32 v11, v28, v11
	ds_read_b32 v60, v11
	ds_read_b32 v173, v179 offset:43520
	v_or_b32_e32 v11, 14, v9
	v_xor_b32_e32 v176, 49, v9
	v_cndmask_b32_e32 v63, v176, v11, vcc
	v_lshl_or_b32 v11, v63, 8, v10
	v_add_u32_e32 v178, v111, v11
	v_add_u32_e32 v11, v28, v11
	ds_read_b32 v61, v11
	ds_read_b32 v174, v178 offset:43520
	v_or_b32_e32 v11, 15, v9
	v_xor_b32_e32 v177, 48, v9
	v_cndmask_b32_e32 v65, v177, v11, vcc
	v_lshl_or_b32 v11, v65, 8, v10
	v_add_u32_e32 v179, v111, v11
	v_add_u32_e32 v11, v28, v11
	ds_read_b32 v32, v11
	ds_read_b32 v175, v179 offset:43520
	v_and_b32_e32 v9, 0x3fffff00, v30
	v_lshlrev_b32_e32 v10, 6, v8
	v_cmp_ne_u32_e32 vcc, 0, v8
	v_or3_b32 v9, v10, v9, v31
	s_waitcnt lgkmcnt(0)
	v_fmac_f32_e32 v22, 0, v17
	v_fmac_f32_e32 v15, v22, v161
	v_mul_f32_e32 v13, v17, v161
	v_fmac_f32_e32 v16, v15, v162
	v_mul_f32_e32 v14, v13, v162
	v_fmac_f32_e32 v18, v16, v163
	v_mul_f32_e32 v38, v14, v163
	v_fmac_f32_e32 v33, v18, v164
	v_mul_f32_e32 v23, v38, v164
	v_fmac_f32_e32 v34, v33, v165
	v_mul_f32_e32 v24, v23, v165
	v_fmac_f32_e32 v35, v34, v166
	v_mul_f32_e32 v47, v24, v166
	v_fmac_f32_e32 v42, v35, v167
	v_mul_f32_e32 v40, v47, v167
	v_fmac_f32_e32 v43, v42, v168
	v_mul_f32_e32 v41, v40, v168
	v_fmac_f32_e32 v44, v43, v169
	v_mul_f32_e32 v56, v41, v169
	v_fmac_f32_e32 v51, v44, v170
	v_mul_f32_e32 v49, v56, v170
	v_fmac_f32_e32 v52, v51, v171
	v_mul_f32_e32 v50, v49, v171
	v_fmac_f32_e32 v53, v52, v172
	v_mul_f32_e32 v64, v50, v172
	v_fmac_f32_e32 v60, v53, v173
	v_mul_f32_e32 v58, v64, v173
	v_fmac_f32_e32 v61, v60, v174
	v_mul_f32_e32 v59, v58, v174
	v_fmac_f32_e32 v32, v61, v175
	v_mul_f32_e32 v66, v59, v175
	v_lshlrev_b32_e32 v9, 2, v9
	v_add_u32_e32 v10, v27, v9
	v_add_u32_e32 v9, v29, v9
	ds_write_b32 v10, v66
	ds_write_b32 v9, v32
	s_waitcnt lgkmcnt(0)
	s_barrier
	s_and_saveexec_b64 s[0:1], vcc
	s_cbranch_execz .LBB0_372
	v_lshlrev_b32_e32 v9, 2, v30
	v_and_b32_e32 v9, 0xfffffcfc, v9
	v_add_u32_e32 v10, v29, v9
	v_add_u32_e32 v9, v27, v9
	ds_read_b32 v67, v9
	ds_read_b32 v68, v10
	s_waitcnt lgkmcnt(0)
	v_fmac_f32_e32 v68, 0, v67
